# batch8: + P5 z gate pieces loaded one head ahead
# baseline (speedup 1.0000x reference)
.LBB0_563:
	s_lshr_b32 s0, s49, 3
	s_and_b32 s6, s0, 63
	v_readlane_b32 s0, v255, 55
	s_and_b32 s0, s0, 7
	v_readlane_b32 s56, v253, 18
	v_lshl_or_b32 v2, s0, 9, v165
	v_readlane_b32 s8, v255, 53
	v_lshlrev_b32_e32 v160, 1, v2
	v_lshlrev_b32_e32 v12, 2, v2
	v_mov_b32_e32 v13, v161
	v_readlane_b32 s66, v253, 28
	v_readlane_b32 s67, v253, 29
	v_readlane_b32 s9, v255, 54
	v_cndmask_b32_e64 v2, v1, 0, s[80:81]
	v_lshl_add_u64 v[110:111], s[66:67], 0, v[12:13]
	v_lshl_add_u64 v[112:113], s[8:9], 0, v[12:13]
	v_cndmask_b32_e64 v1, v205, 0, s[80:81]
	v_cndmask_b32_e64 v12, v206, 0, s[80:81]
	v_lshlrev_b32_e32 v13, 16, v2
	v_fma_f32 v13, v176, v13, v184
	v_and_b32_e32 v70, 0xffff0000, v2
	v_lshlrev_b32_e32 v81, 16, v1
	v_lshlrev_b32_e32 v85, 16, v12
	v_lshlrev_b32_e32 v84, 16, v3
	v_mov_b32_e32 v74, v182
	v_mov_b32_e32 v75, v180
	v_fma_f32 v80, v177, v70, v185
	v_fmac_f32_e32 v13, v178, v81
	v_pk_mul_f32 v[70:71], v[74:75], v[84:85]
	v_and_b32_e32 v83, 0xffff0000, v1
	v_add_f32_e32 v13, v71, v13
	v_add_f32_e32 v13, v70, v13
	v_mul_f32_e32 v70, 0xbfb8aa3b, v13
	v_exp_f32_e32 v82, v70
	v_and_b32_e32 v91, 0xffff0000, v12
	v_and_b32_e32 v90, 0xffff0000, v3
	v_mov_b32_e32 v92, v183
	v_add_f32_e32 v82, 1.0, v82
	v_rcp_f32_e32 v82, v82
	v_mov_b32_e32 v93, v181
	v_fmac_f32_e32 v80, v179, v83
	v_pk_mul_f32 v[94:95], v[92:93], v[90:91]
	v_mul_f32_e32 v13, v13, v82
	v_add_f32_e32 v80, v95, v80
	v_add_f32_e32 v82, v94, v80
	v_mul_f32_e32 v80, 0xbfb8aa3b, v82
	v_exp_f32_e32 v80, v80
	ds_read_b128 v[76:79], v242
	ds_read_b128 v[70:73], v242 offset:16
	v_mov_b32_e32 v94, v178
	v_mov_b32_e32 v95, v176
	v_add_f32_e32 v80, 1.0, v80
	v_rcp_f32_e32 v98, v80
	v_mov_b32_e32 v80, v85
	v_lshlrev_b32_e32 v87, 16, v4
	v_lshlrev_b32_e32 v86, 16, v5
	v_pk_mul_f32 v[80:81], v[94:95], v[80:81]
	v_mul_f32_e32 v82, v82, v98
	s_waitcnt lgkmcnt(1)
	v_mul_f32_e32 v13, v13, v76
	v_pk_mul_f32 v[96:97], v[94:95], v[84:85]
	v_mul_f32_e32 v106, v82, v76
	v_pk_mov_b32 v[84:85], v[86:87], v[84:85] op_sel:[1,0]
	v_add_f32_e32 v76, v81, v184
	v_pk_mul_f32 v[104:105], v[74:75], v[84:85]
	v_add_f32_e32 v76, v80, v76
	v_add_f32_e32 v76, v105, v76
	v_add_f32_e32 v76, v104, v76
	v_mul_f32_e32 v80, 0xbfb8aa3b, v76
	v_add_f32_e32 v97, v97, v184
	v_exp_f32_e32 v104, v80
	v_pk_mul_f32 v[80:81], v[74:75], v[86:87]
	v_add_f32_e32 v96, v96, v97
	v_add_f32_e32 v81, v81, v96
	v_add_f32_e32 v96, v80, v81
	v_mul_f32_e32 v80, 0xbfb8aa3b, v96
	v_exp_f32_e32 v80, v80
	v_add_f32_e32 v97, 1.0, v104
	v_rcp_f32_e32 v97, v97
	v_mov_b32_e32 v98, v179
	v_add_f32_e32 v80, 1.0, v80
	v_rcp_f32_e32 v104, v80
	v_mov_b32_e32 v99, v177
	v_mov_b32_e32 v82, v91
	v_mul_f32_e32 v76, v76, v97
	v_and_b32_e32 v89, 0xffff0000, v4
	v_and_b32_e32 v88, 0xffff0000, v5
	v_pk_mul_f32 v[82:83], v[98:99], v[82:83]
	v_mul_f32_e32 v105, v76, v77
	v_mul_f32_e32 v76, v96, v104
	v_pk_mul_f32 v[100:101], v[98:99], v[90:91]
	v_mul_f32_e32 v104, v76, v78
	v_pk_mov_b32 v[90:91], v[88:89], v[90:91] op_sel:[1,0]
	v_add_f32_e32 v76, v83, v185
	v_pk_mul_f32 v[96:97], v[92:93], v[90:91]
	v_add_f32_e32 v76, v82, v76
	v_add_f32_e32 v76, v97, v76
	v_add_f32_e32 v76, v96, v76
	v_mul_f32_e32 v82, 0xbfb8aa3b, v76
	v_add_f32_e32 v97, v101, v185
	v_exp_f32_e32 v96, v82
	v_pk_mul_f32 v[82:83], v[92:93], v[88:89]
	v_add_f32_e32 v97, v100, v97
	v_add_f32_e32 v83, v83, v97
	v_add_f32_e32 v97, v82, v83
	v_mul_f32_e32 v82, 0xbfb8aa3b, v97
	v_exp_f32_e32 v100, v82
	v_pk_mul_f32 v[82:83], v[94:95], v[84:85]
	v_add_f32_e32 v84, 1.0, v96
	v_rcp_f32_e32 v96, v84
	v_add_f32_e32 v84, 1.0, v100
	v_rcp_f32_e32 v100, v84
	v_lshlrev_b32_e32 v103, 16, v6
	v_mul_f32_e32 v76, v76, v96
	v_lshlrev_b32_e32 v102, 16, v7
	v_mul_f32_e32 v107, v76, v77
	v_mul_f32_e32 v76, v97, v100
	v_pk_mul_f32 v[84:85], v[94:95], v[86:87]
	v_mul_f32_e32 v108, v76, v78
	v_pk_mov_b32 v[86:87], v[102:103], v[86:87] op_sel:[1,0]
	v_add_f32_e32 v78, v83, v184
	v_pk_mul_f32 v[100:101], v[74:75], v[86:87]
	v_add_f32_e32 v78, v82, v78
	v_add_f32_e32 v78, v101, v78
	v_add_f32_e32 v78, v100, v78
	v_mul_f32_e32 v82, 0xbfb8aa3b, v78
	v_add_f32_e32 v85, v85, v184
	v_exp_f32_e32 v100, v82
	v_pk_mul_f32 v[82:83], v[74:75], v[102:103]
	v_add_f32_e32 v84, v84, v85
	v_add_f32_e32 v83, v83, v84
	v_add_f32_e32 v84, v82, v83
	v_mul_f32_e32 v82, 0xbfb8aa3b, v84
	v_exp_f32_e32 v82, v82
	v_add_f32_e32 v85, 1.0, v100
	v_rcp_f32_e32 v85, v85
	v_and_b32_e32 v81, 0xffff0000, v6
	v_add_f32_e32 v82, 1.0, v82
	v_rcp_f32_e32 v100, v82
	v_and_b32_e32 v80, 0xffff0000, v7
	v_pk_mul_f32 v[76:77], v[98:99], v[90:91]
	v_mul_f32_e32 v78, v78, v85
	v_mul_f32_e32 v101, v78, v79
	v_mul_f32_e32 v78, v84, v100
	v_pk_mul_f32 v[84:85], v[94:95], v[86:87]
	v_pk_mov_b32 v[86:87], v[80:81], v[88:89] op_sel:[1,0]
	v_add_f32_e32 v77, v77, v185
	v_pk_mul_f32 v[90:91], v[98:99], v[88:89]
	v_pk_mul_f32 v[88:89], v[92:93], v[86:87]
	v_add_f32_e32 v76, v76, v77
	v_add_f32_e32 v76, v89, v76
	s_waitcnt lgkmcnt(0)
	v_mul_f32_e32 v100, v78, v70
	v_add_f32_e32 v78, v88, v76
	v_mul_f32_e32 v76, 0xbfb8aa3b, v78
	v_add_f32_e32 v89, v91, v185
	v_exp_f32_e32 v88, v76
	v_pk_mul_f32 v[76:77], v[92:93], v[80:81]
	v_add_f32_e32 v89, v90, v89
	v_add_f32_e32 v77, v77, v89
	v_add_f32_e32 v109, v76, v77
	v_mul_f32_e32 v76, 0xbfb8aa3b, v109
	v_exp_f32_e32 v89, v76
	v_add_f32_e32 v88, 1.0, v88
	v_lshlrev_b32_e32 v97, 16, v8
	v_lshlrev_b32_e32 v96, 16, v9
	v_rcp_f32_e32 v114, v88
	v_add_f32_e32 v88, 1.0, v89
	v_rcp_f32_e32 v115, v88
	v_pk_mov_b32 v[88:89], v[96:97], v[102:103] op_sel:[1,0]
	v_add_f32_e32 v85, v85, v184
	v_pk_mul_f32 v[90:91], v[74:75], v[88:89]
	v_add_f32_e32 v84, v84, v85
	v_add_f32_e32 v84, v91, v84
	v_add_f32_e32 v90, v90, v84
	v_mul_f32_e32 v84, 0xbfb8aa3b, v90
	v_exp_f32_e32 v84, v84
	v_mul_f32_e32 v78, v78, v114
	v_mul_f32_e32 v91, v78, v79
	v_mul_f32_e32 v78, v109, v115
	v_add_f32_e32 v79, 1.0, v84
	v_and_b32_e32 v83, 0xffff0000, v8
	v_and_b32_e32 v82, 0xffff0000, v9
	v_pk_mul_f32 v[76:77], v[94:95], v[102:103]
	v_rcp_f32_e32 v102, v79
	v_mul_f32_e32 v103, v78, v70
	v_pk_mul_f32 v[78:79], v[98:99], v[86:87]
	v_pk_mul_f32 v[84:85], v[98:99], v[80:81]
	v_pk_mov_b32 v[80:81], v[82:83], v[80:81] op_sel:[1,0]
	v_add_f32_e32 v79, v79, v185
	v_pk_mul_f32 v[86:87], v[92:93], v[80:81]
	v_add_f32_e32 v78, v78, v79
	v_add_f32_e32 v78, v87, v78
	v_add_f32_e32 v86, v86, v78
	v_mul_f32_e32 v78, 0xbfb8aa3b, v86
	v_exp_f32_e32 v87, v78
	v_mul_f32_e32 v70, v90, v102
	v_mul_f32_e32 v90, v70, v71
	v_add_f32_e32 v70, v77, v184
	v_add_f32_e32 v77, 1.0, v87
	v_rcp_f32_e32 v77, v77
	v_pk_mul_f32 v[78:79], v[74:75], v[96:97]
	v_add_f32_e32 v70, v76, v70
	v_add_f32_e32 v70, v79, v70
	v_add_f32_e32 v70, v78, v70
	v_mul_f32_e32 v78, v86, v77
	v_pk_mul_f32 v[76:77], v[92:93], v[82:83]
	v_mul_f32_e32 v83, 0xbfb8aa3b, v70
	v_exp_f32_e32 v83, v83
	v_add_f32_e32 v79, v85, v185
	v_add_f32_e32 v79, v84, v79
	v_add_f32_e32 v77, v77, v79
	v_add_f32_e32 v84, v76, v77
	v_add_f32_e32 v76, 1.0, v83
	v_rcp_f32_e32 v76, v76
	v_mul_f32_e32 v77, 0xbfb8aa3b, v84
	v_exp_f32_e32 v77, v77
	v_mul_f32_e32 v83, v78, v71
	v_mul_f32_e32 v70, v70, v76
	v_mul_f32_e32 v85, v70, v72
	v_add_f32_e32 v70, 1.0, v77
	v_rcp_f32_e32 v86, v70
	v_pk_mul_f32 v[70:71], v[94:95], v[88:89]
	v_lshlrev_b32_e32 v78, 16, v10
	v_mov_b32_e32 v79, v96
	v_add_f32_e32 v71, v71, v184
	v_pk_mul_f32 v[74:75], v[74:75], v[78:79]
	v_add_f32_e32 v70, v70, v71
	v_pk_mul_f32 v[76:77], v[98:99], v[80:81]
	v_add_f32_e32 v70, v75, v70
	v_add_f32_e32 v74, v74, v70
	v_and_b32_e32 v70, 0xffff0000, v10
	v_mov_b32_e32 v71, v82
	v_add_f32_e32 v75, v77, v185
	v_pk_mul_f32 v[70:71], v[92:93], v[70:71]
	v_add_f32_e32 v75, v76, v75
	v_add_f32_e32 v71, v71, v75
	v_add_f32_e32 v70, v70, v71
	v_mul_f32_e32 v75, 0xbfb8aa3b, v70
	v_mul_f32_e32 v71, 0xbfb8aa3b, v74
	v_exp_f32_e32 v75, v75
	v_exp_f32_e32 v71, v71
	s_lshl_b32 s1, s6, 7
	s_add_i32 s6, s5, s6
	v_add_f32_e32 v75, 1.0, v75
	v_add_f32_e32 v71, 1.0, v71
	v_rcp_f32_e32 v75, v75
	v_rcp_f32_e32 v71, v71
	s_ashr_i32 s7, s6, 31
	s_lshl_b64 s[6:7], s[6:7], 20
	v_mul_f32_e32 v70, v70, v75
	v_mul_f32_e32 v76, v84, v86
	v_mul_f32_e32 v71, v74, v71
	v_mul_f32_e32 v78, v70, v73
	v_cvt_pk_bf16_f32 v70, v13, v105
	v_or_b32_e32 v13, s6, v170
	s_add_i32 s1, s1, s4
	v_mul_f32_e32 v77, v76, v72
	v_mul_f32_e32 v74, v71, v73
	v_cvt_pk_bf16_f32 v71, v104, v101
	v_cvt_pk_bf16_f32 v72, v100, v90
	v_cvt_pk_bf16_f32 v73, v85, v74
	v_lshl_or_b32 v114, s0, 17, v13
	v_add_u32_e32 v13, s1, v211
	v_cvt_pk_bf16_f32 v74, v106, v107
	v_cvt_pk_bf16_f32 v75, v108, v91
	v_cvt_pk_bf16_f32 v76, v103, v83
	v_cvt_pk_bf16_f32 v77, v77, v78
	ds_write_b128 v227, v[70:73]
	ds_write_b128 v227, v[74:77] offset:272
	ds_write_b128 v229, v[14:17]
	ds_write_b128 v231, v[18:21]
	v_mad_i64_i32 v[70:71], s[4:5], v13, s11, v[160:161]
	v_add_u32_e32 v13, s1, v171
	v_mov_b32_e32 v115, s7
	s_mov_b64 s[6:7], 0x45c00080
	v_mad_i64_i32 v[118:119], s[4:5], v13, s11, v[160:161]
	v_add_u32_e32 v13, s1, v204
	v_lshl_add_u64 v[116:117], v[70:71], 0, s[6:7]
	v_mad_i64_i32 v[70:71], s[4:5], v13, s11, v[160:161]
	v_add_u32_e32 v13, s1, v163
	v_lshl_add_u64 v[120:121], v[70:71], 0, s[6:7]
	v_mad_i64_i32 v[70:71], s[4:5], v13, s11, v[160:161]
	v_add_u32_e32 v13, s1, v173
	v_lshl_add_u64 v[122:123], v[70:71], 0, s[6:7]
	v_mad_i64_i32 v[70:71], s[4:5], v13, s11, v[160:161]
	v_lshl_add_u64 v[124:125], v[70:71], 0, s[6:7]
	v_add_u32_e32 v70, s1, v232
	v_ashrrev_i32_e32 v71, 31, v70
	v_lshlrev_b64 v[126:127], 13, v[70:71]
	v_or_b32_e32 v13, v162, v126
	s_mov_b32 s2, 0
	v_lshl_or_b32 v126, s0, 10, v13
	v_lshl_add_u64 v[198:199], s[92:93], 0, v[126:127]
	v_add_co_u32_e32 v198, vcc, 0x3dc00000, v198
	s_nop 1
	v_addc_co_u32_e32 v199, vcc, 0, v199, vcc
	global_load_dwordx4 v[200:203], v[198:199], off
	global_load_dwordx4 v[216:219], v[198:199], off offset:64
	v_mov_b32_e32 v140, 0
	s_mov_b64 s[0:1], 0
	v_mov_b32_e32 v13, v245
	v_mov_b32_e32 v141, v244
	v_mov_b32_e32 v142, v243
	v_readlane_b32 s57, v253, 19
	v_readlane_b32 s58, v253, 20
	v_readlane_b32 s59, v253, 21
	v_readlane_b32 s60, v253, 22
	v_readlane_b32 s61, v253, 23
	v_readlane_b32 s62, v253, 24
	v_readlane_b32 s63, v253, 25
	v_readlane_b32 s64, v253, 26
	v_readlane_b32 s65, v253, 27
	v_readlane_b32 s68, v253, 30
	v_readlane_b32 s69, v253, 31
	v_readlane_b32 s70, v253, 32
	v_readlane_b32 s71, v253, 33
	s_waitcnt lgkmcnt(0)
	s_barrier
	s_waitcnt vmcnt(0)
	s_branch .LBB0_565

.LBB0_565:
	v_lshl_add_u64 v[128:129], s[92:93], 0, v[126:127]
	s_mov_b32 s4, 0x3dc00000
	v_add_co_u32_e32 v198, vcc, s4, v128
	v_readlane_b32 s6, v11, s2
	s_nop 0
	v_addc_co_u32_e32 v199, vcc, 0, v129, vcc
	v_mov_b64_e32 v[74:75], v[200:201]
	v_mov_b64_e32 v[76:77], v[202:203]
	v_mov_b64_e32 v[70:71], v[216:217]
	v_mov_b64_e32 v[72:73], v[218:219]
	global_load_dwordx4 v[200:203], v[198:199], off offset:128
	global_load_dwordx4 v[216:219], v[198:199], off offset:192
	ds_read2st64_b32 v[130:131], v13 offset1:16
	s_and_b32 s52, s2, 1
	s_add_i32 s51, 0, 0xa800
	s_cmp_eq_u32 s52, 0
	s_cselect_b64 s[90:91], -1, 0
	s_waitcnt lgkmcnt(0)
	v_div_scale_f32 v102, s[4:5], v130, v130, s6
	v_rcp_f32_e32 v103, v102
	s_and_b64 s[4:5], s[90:91], exec
	s_cselect_b32 s4, s33, s51
	v_lshlrev_b32_e32 v143, 1, v164
	v_fma_f32 v78, -v102, v103, 1.0
	v_fmac_f32_e32 v103, v78, v103
	v_add3_u32 v78, s4, v222, v143
	v_add_u32_e32 v79, 0x1000, v78
	v_div_scale_f32 v104, vcc, s6, v130, s6
	ds_read_b128 v[94:97], v141
	ds_read_b128 v[98:101], v141 offset:64
	ds_read2_b64 v[90:93], v78 offset1:4
	ds_read2_b64 v[86:89], v79 offset0:32 offset1:36
	v_add_u32_e32 v79, 0x2000, v78
	v_add_u32_e32 v78, 0x3000, v78
	v_mul_f32_e32 v105, v104, v103
	ds_read2_b64 v[82:85], v79 offset0:64 offset1:68
	ds_read2_b64 v[78:81], v78 offset0:96 offset1:100
	v_fma_f32 v106, -v102, v105, v104
	v_fmac_f32_e32 v105, v106, v103
	v_fma_f32 v102, -v102, v105, v104
	v_div_fmas_f32 v132, v102, v103, v105
	s_waitcnt lgkmcnt(5)
	v_sub_f32_e32 v109, v131, v94
	s_mov_b64 s[4:5], -1
	s_and_b64 vcc, exec, s[82:83]
	s_waitcnt lgkmcnt(4)
	v_sub_f32_e32 v107, v131, v98
	v_sub_f32_e32 v108, v131, v95
	v_sub_f32_e32 v106, v131, v99
	v_sub_f32_e32 v105, v131, v96
	v_sub_f32_e32 v104, v131, v100
	v_sub_f32_e32 v103, v131, v97
	v_sub_f32_e32 v102, v131, v101
	s_cbranch_vccnz .LBB0_567
	v_mul_f32_e32 v95, 0x3fb8aa3b, v107
	v_mul_f32_e32 v99, 0x3fb8aa3b, v104
	v_mul_f32_e32 v94, 0x3fb8aa3b, v109
	v_exp_f32_e32 v96, v95
	v_mul_f32_e32 v95, 0x3fb8aa3b, v108
	v_mul_f32_e32 v97, 0x3fb8aa3b, v106
	v_mul_f32_e32 v98, 0x3fb8aa3b, v105
	v_exp_f32_e32 v100, v99
	v_mul_f32_e32 v99, 0x3fb8aa3b, v103
	v_mul_f32_e32 v101, 0x3fb8aa3b, v102
	v_exp_f32_e32 v94, v94
	v_exp_f32_e32 v95, v95
	v_exp_f32_e32 v97, v97
	v_exp_f32_e32 v98, v98
	v_exp_f32_e32 v99, v99
	v_exp_f32_e32 v101, v101
	v_pk_mul_f32 v[94:95], v[38:39], v[94:95]
	v_pk_mul_f32 v[96:97], v[46:47], v[96:97]
	v_pk_mul_f32 v[98:99], v[40:41], v[98:99]
	v_pk_mul_f32 v[100:101], v[48:49], v[100:101]
	s_mov_b64 s[4:5], 0

.LBB0_574:
	s_and_b64 s[6:7], s[90:91], exec
	s_mov_b32 s6, 0xec00
	s_cselect_b32 s6, 0x17400, s6
	s_add_i32 s6, s6, 0
	v_add3_u32 v130, s6, v162, v222
	ds_read_b128 v[94:97], v130
	ds_read_b128 v[98:101], v130 offset:64
	ds_read_b128 v[102:105], v130 offset:4352
	ds_read_b128 v[106:109], v130 offset:4416
	ds_read_b128 v[132:135], v130 offset:8704
	ds_read_b128 v[136:139], v130 offset:8768
	ds_read_b128 v[144:147], v130 offset:13056
	ds_read_b128 v[148:151], v130 offset:13120
	s_waitcnt lgkmcnt(7)
	v_mfma_f32_16x16x32_bf16 v[94:97], v[94:97], v[22:25], 0
	s_waitcnt lgkmcnt(5)
	v_mfma_f32_16x16x32_bf16 v[102:105], v[102:105], v[22:25], 0
	s_waitcnt lgkmcnt(3)
	v_mfma_f32_16x16x32_bf16 v[132:135], v[132:135], v[22:25], 0
	s_waitcnt lgkmcnt(1)
	v_mfma_f32_16x16x32_bf16 v[144:147], v[144:147], v[22:25], 0
	ds_read_b128 v[152:155], v130 offset:128
	ds_read_b128 v[186:189], v130 offset:4480
	ds_read_b128 v[190:193], v130 offset:8832
	ds_read_b128 v[194:197], v130 offset:13184
	v_mfma_f32_16x16x32_bf16 v[94:97], v[98:101], v[26:29], v[94:97]
	v_mfma_f32_16x16x32_bf16 v[98:101], v[106:109], v[26:29], v[102:105]
	s_waitcnt lgkmcnt(4)
	v_mfma_f32_16x16x32_bf16 v[106:109], v[148:151], v[26:29], v[144:147]
	v_mfma_f32_16x16x32_bf16 v[102:105], v[136:139], v[26:29], v[132:135]
	s_nop 2
	ds_read_b128 v[132:135], v130 offset:192
	ds_read_b128 v[136:139], v130 offset:4544
	ds_read_b128 v[144:147], v130 offset:8896
	ds_read_b128 v[148:151], v130 offset:13248
	s_waitcnt lgkmcnt(7)
	v_mfma_f32_16x16x32_bf16 v[94:97], v[152:155], v[30:33], v[94:97]
	s_waitcnt lgkmcnt(6)
	v_mfma_f32_16x16x32_bf16 v[98:101], v[186:189], v[30:33], v[98:101]
	s_waitcnt lgkmcnt(4)
	v_mfma_f32_16x16x32_bf16 v[106:109], v[194:197], v[30:33], v[106:109]
	v_mfma_f32_16x16x32_bf16 v[152:155], v[190:193], v[30:33], v[102:105]
	s_waitcnt lgkmcnt(3)
	v_mfma_f32_16x16x32_bf16 v[132:135], v[132:135], v[34:37], v[94:97]
	s_waitcnt lgkmcnt(2)
	v_mfma_f32_16x16x32_bf16 v[102:105], v[136:139], v[34:37], v[98:101]
	s_waitcnt lgkmcnt(1)
	v_mfma_f32_16x16x32_bf16 v[98:101], v[144:147], v[34:37], v[152:155]
	s_waitcnt lgkmcnt(0)
	v_mfma_f32_16x16x32_bf16 v[94:97], v[148:151], v[34:37], v[106:109]
	s_nop 2
	v_mul_f32_e32 v106, 0x3fb8aa3b, v131
	s_cmpk_eq_i32 s0, 0x700
	s_cbranch_scc1 .Lp5_zw_last
	s_waitcnt vmcnt(20)
	s_branch .Lp5_zw_done
.Lp5_zw_last:
	s_waitcnt vmcnt(2)
